# speedup vs baseline: 1.0407x; 1.0060x over previous
_ZN12_GLOBAL__N_17k_pairsEPKDF16_PKiS1_PKfS5_S5_Pf:
	s_cmpk_gt_u32 s2, 0x2ff
	s_cbranch_scc1 .Lpairs_exit
	s_load_dwordx8 s[4:11], s[0:1], 0x0
	s_load_dwordx4 s[12:15], s[0:1], 0x20
	s_load_dwordx2 s[16:17], s[0:1], 0x30
	v_lshrrev_b32_e32 v2, 6, v0
	v_and_b32_e32 v1, 15, v0
	v_lshlrev_b32_e32 v72, 4, v0
	v_readfirstlane_b32 s3, v2
	s_lshl_b32 s32, s2, 3
	s_add_i32 s32, s32, s3
	s_add_i32 s33, s32, 0x1800
	s_add_i32 s34, s33, 0x1800
	v_lshlrev_b32_e32 v77, 3, v1
	v_add_u32_e32 v73, 0x2000, v72
	v_and_b32_e32 v76, 48, v0
	v_lshlrev_b32_e32 v3, 2, v1
	s_waitcnt lgkmcnt(0)
	s_min_i32 s3, s32, 0x30d3
	s_lshl_b32 s3, s3, 7
	s_add_u32 s24, s6, s3
	s_addc_u32 s25, s7, 0
	global_load_dwordx2 v[68:69], v77, s[24:25] nt
	s_min_i32 s3, s33, 0x30d3
	s_lshl_b32 s3, s3, 7
	s_add_u32 s24, s6, s3
	s_addc_u32 s25, s7, 0
	global_load_dwordx2 v[74:75], v77, s[24:25] nt
	global_load_dwordx4 v[52:55], v72, s[8:9]
	global_load_dwordx4 v[56:59], v73, s[8:9]
	s_load_dword s18, s[14:15], 0x0
	global_load_dword v4, v3, s[12:13] offset:0
	global_load_dword v8, v3, s[10:11] offset:0
	global_load_dword v5, v3, s[12:13] offset:64
	global_load_dword v9, v3, s[10:11] offset:64
	global_load_dword v6, v3, s[12:13] offset:128
	global_load_dword v10, v3, s[10:11] offset:128
	global_load_dword v7, v3, s[12:13] offset:192
	global_load_dword v11, v3, s[10:11] offset:192
	v_and_b32_e32 v2, 63, v0
	v_lshlrev_b32_e32 v2, 4, v2
	v_cmp_eq_u32_e64 s[20:21], 1, v1
	v_cmp_eq_u32_e64 s[22:23], 2, v1
	v_cmp_eq_u32_e64 s[26:27], 3, v1
	v_cmp_gt_u32_e64 s[28:29], 4, v1
	v_add_u32_e32 v0, v76, v3
	s_waitcnt vmcnt(10)
	v_lshl_or_b32 v70, v68, 7, v76
	v_lshl_or_b32 v71, v69, 7, v76
	global_load_dwordx4 v[20:23], v70, s[4:5]
	global_load_dwordx4 v[24:27], v70, s[4:5] offset:64
	global_load_dwordx4 v[28:31], v71, s[4:5]
	global_load_dwordx4 v[32:35], v71, s[4:5] offset:64
	v_lshl_or_b32 v70, v74, 7, v76
	v_lshl_or_b32 v71, v75, 7, v76
	global_load_dwordx4 v[36:39], v70, s[4:5]
	global_load_dwordx4 v[40:43], v70, s[4:5] offset:64
	global_load_dwordx4 v[44:47], v71, s[4:5]
	global_load_dwordx4 v[48:51], v71, s[4:5] offset:64
	s_cmpk_lt_i32 s34, 0x30d4
	s_cbranch_scc0 .Lpairs_no3a
	s_min_i32 s3, s34, 0x30d3
	s_lshl_b32 s3, s3, 7
	s_add_u32 s24, s6, s3
	s_addc_u32 s25, s7, 0
	global_load_dwordx2 v[68:69], v77, s[24:25] nt
.Lpairs_no3a:
	s_waitcnt vmcnt(16)
	ds_write_b128 v72, v[52:55]
	ds_write_b128 v72, v[56:59] offset:8192
	s_waitcnt lgkmcnt(0)
	s_barrier
	s_mov_b32 s36, s32
	s_mov_b32 s37, 2
	s_cmpk_lt_i32 s34, 0x30d4
	s_cselect_b32 s37, 3, s37
	s_mov_b32 s38, 0
	s_waitcnt vmcnt(4)
.Lpairs_loop:
	ds_read_b128 v[52:55], v2 offset:0
	ds_read_b128 v[56:59], v2 offset:1024
	ds_read_b128 v[60:63], v2 offset:2048
	ds_read_b128 v[64:67], v2 offset:3072
	s_waitcnt lgkmcnt(3)
	v_mfma_f32_16x16x32_f16 v[16:19], v[20:23], v[52:55], 0
	ds_read_b128 v[52:55], v2 offset:4096
	s_waitcnt lgkmcnt(3)
	v_mfma_f32_16x16x32_f16 v[16:19], v[24:27], v[56:59], v[16:19]
	ds_read_b128 v[56:59], v2 offset:5120
	s_waitcnt lgkmcnt(3)
	v_mfma_f32_16x16x32_f16 v[16:19], v[28:31], v[60:63], v[16:19]
	ds_read_b128 v[60:63], v2 offset:6144
	s_waitcnt lgkmcnt(3)
	v_mfma_f32_16x16x32_f16 v[16:19], v[32:35], v[64:67], v[16:19]
	ds_read_b128 v[64:67], v2 offset:7168
	s_nop 7
	v_add_f32_e32 v16, v4, v16
	v_add_f32_e32 v17, v4, v17
	v_add_f32_e32 v18, v4, v18
	v_add_f32_e32 v19, v4, v19
	v_max_f32_e32 v16, 0, v16
	v_max_f32_e32 v17, 0, v17
	v_max_f32_e32 v18, 0, v18
	v_max_f32_e32 v19, 0, v19
	v_mul_f32_e32 v12, v8, v16
	v_mul_f32_e32 v13, v8, v17
	v_mul_f32_e32 v14, v8, v18
	v_mul_f32_e32 v15, v8, v19
	s_waitcnt lgkmcnt(3)
	v_mfma_f32_16x16x32_f16 v[16:19], v[20:23], v[52:55], 0
	ds_read_b128 v[52:55], v2 offset:8192
	s_waitcnt lgkmcnt(3)
	v_mfma_f32_16x16x32_f16 v[16:19], v[24:27], v[56:59], v[16:19]
	ds_read_b128 v[56:59], v2 offset:9216
	s_waitcnt lgkmcnt(3)
	v_mfma_f32_16x16x32_f16 v[16:19], v[28:31], v[60:63], v[16:19]
	ds_read_b128 v[60:63], v2 offset:10240
	s_waitcnt lgkmcnt(3)
	v_mfma_f32_16x16x32_f16 v[16:19], v[32:35], v[64:67], v[16:19]
	ds_read_b128 v[64:67], v2 offset:11264
	s_nop 7
	v_add_f32_e32 v16, v5, v16
	v_add_f32_e32 v17, v5, v17
	v_add_f32_e32 v18, v5, v18
	v_add_f32_e32 v19, v5, v19
	v_max_f32_e32 v16, 0, v16
	v_max_f32_e32 v17, 0, v17
	v_max_f32_e32 v18, 0, v18
	v_max_f32_e32 v19, 0, v19
	v_fmac_f32_e32 v12, v9, v16
	v_fmac_f32_e32 v13, v9, v17
	v_fmac_f32_e32 v14, v9, v18
	v_fmac_f32_e32 v15, v9, v19
	s_waitcnt lgkmcnt(3)
	v_mfma_f32_16x16x32_f16 v[16:19], v[20:23], v[52:55], 0
	ds_read_b128 v[52:55], v2 offset:12288
	s_waitcnt lgkmcnt(3)
	v_mfma_f32_16x16x32_f16 v[16:19], v[24:27], v[56:59], v[16:19]
	ds_read_b128 v[56:59], v2 offset:13312
	s_waitcnt lgkmcnt(3)
	v_mfma_f32_16x16x32_f16 v[16:19], v[28:31], v[60:63], v[16:19]
	ds_read_b128 v[60:63], v2 offset:14336
	s_waitcnt lgkmcnt(3)
	v_mfma_f32_16x16x32_f16 v[16:19], v[32:35], v[64:67], v[16:19]
	ds_read_b128 v[64:67], v2 offset:15360
	s_nop 7
	v_add_f32_e32 v16, v6, v16
	v_add_f32_e32 v17, v6, v17
	v_add_f32_e32 v18, v6, v18
	v_add_f32_e32 v19, v6, v19
	v_max_f32_e32 v16, 0, v16
	v_max_f32_e32 v17, 0, v17
	v_max_f32_e32 v18, 0, v18
	v_max_f32_e32 v19, 0, v19
	v_fmac_f32_e32 v12, v10, v16
	v_fmac_f32_e32 v13, v10, v17
	v_fmac_f32_e32 v14, v10, v18
	v_fmac_f32_e32 v15, v10, v19
	s_waitcnt lgkmcnt(3)
	v_mfma_f32_16x16x32_f16 v[16:19], v[20:23], v[52:55], 0
	s_waitcnt lgkmcnt(2)
	v_mfma_f32_16x16x32_f16 v[16:19], v[24:27], v[56:59], v[16:19]
	s_waitcnt lgkmcnt(1)
	v_mfma_f32_16x16x32_f16 v[16:19], v[28:31], v[60:63], v[16:19]
	s_waitcnt lgkmcnt(0)
	v_mfma_f32_16x16x32_f16 v[16:19], v[32:35], v[64:67], v[16:19]
	s_nop 7
	v_add_f32_e32 v16, v7, v16
	v_add_f32_e32 v17, v7, v17
	v_add_f32_e32 v18, v7, v18
	v_add_f32_e32 v19, v7, v19
	v_max_f32_e32 v16, 0, v16
	v_max_f32_e32 v17, 0, v17
	v_max_f32_e32 v18, 0, v18
	v_max_f32_e32 v19, 0, v19
	v_fmac_f32_e32 v12, v11, v16
	v_fmac_f32_e32 v13, v11, v17
	v_fmac_f32_e32 v14, v11, v18
	v_fmac_f32_e32 v15, v11, v19
	v_add_f32_dpp v12, v12, v12 quad_perm:[1,0,3,2] row_mask:0xf bank_mask:0xf
	v_add_f32_dpp v13, v13, v13 quad_perm:[1,0,3,2] row_mask:0xf bank_mask:0xf
	v_add_f32_dpp v14, v14, v14 quad_perm:[1,0,3,2] row_mask:0xf bank_mask:0xf
	v_add_f32_dpp v15, v15, v15 quad_perm:[1,0,3,2] row_mask:0xf bank_mask:0xf
	v_add_f32_dpp v12, v12, v12 quad_perm:[2,3,0,1] row_mask:0xf bank_mask:0xf
	v_add_f32_dpp v13, v13, v13 quad_perm:[2,3,0,1] row_mask:0xf bank_mask:0xf
	v_add_f32_dpp v14, v14, v14 quad_perm:[2,3,0,1] row_mask:0xf bank_mask:0xf
	v_add_f32_dpp v15, v15, v15 quad_perm:[2,3,0,1] row_mask:0xf bank_mask:0xf
	v_add_f32_dpp v12, v12, v12 row_half_mirror row_mask:0xf bank_mask:0xf
	v_add_f32_dpp v13, v13, v13 row_half_mirror row_mask:0xf bank_mask:0xf
	v_add_f32_dpp v14, v14, v14 row_half_mirror row_mask:0xf bank_mask:0xf
	v_add_f32_dpp v15, v15, v15 row_half_mirror row_mask:0xf bank_mask:0xf
	v_add_f32_dpp v12, v12, v12 row_mirror row_mask:0xf bank_mask:0xf
	v_add_f32_dpp v13, v13, v13 row_mirror row_mask:0xf bank_mask:0xf
	v_add_f32_dpp v14, v14, v14 row_mirror row_mask:0xf bank_mask:0xf
	v_add_f32_dpp v15, v15, v15 row_mirror row_mask:0xf bank_mask:0xf
	s_lshl_b32 s3, s36, 6
	s_add_u32 s24, s16, s3
	s_addc_u32 s25, s17, 0
	v_cndmask_b32_e64 v12, v12, v13, s[20:21]
	s_nop 0
	v_cndmask_b32_e64 v12, v12, v14, s[22:23]
	s_nop 0
	v_cndmask_b32_e64 v12, v12, v15, s[26:27]
	s_nop 0
	v_add_f32_e32 v12, s18, v12
	s_mov_b64 s[30:31], exec
	s_mov_b64 exec, s[28:29]
	global_store_dword v0, v12, s[24:25]
	s_mov_b64 exec, s[30:31]
	s_add_i32 s38, s38, 1
	s_cmp_ge_u32 s38, s37
	s_cbranch_scc1 .Lpairs_exit
	s_waitcnt vmcnt(1)
	v_mov_b32_e32 v20, v36
	v_mov_b32_e32 v21, v37
	v_mov_b32_e32 v22, v38
	v_mov_b32_e32 v23, v39
	v_mov_b32_e32 v24, v40
	v_mov_b32_e32 v25, v41
	v_mov_b32_e32 v26, v42
	v_mov_b32_e32 v27, v43
	v_mov_b32_e32 v28, v44
	v_mov_b32_e32 v29, v45
	v_mov_b32_e32 v30, v46
	v_mov_b32_e32 v31, v47
	v_mov_b32_e32 v32, v48
	v_mov_b32_e32 v33, v49
	v_mov_b32_e32 v34, v50
	v_mov_b32_e32 v35, v51
	s_add_i32 s36, s36, 0x1800
	s_cmp_eq_u32 s38, 1
	s_cbranch_scc0 .Lpairs_loop
	s_cmp_eq_u32 s37, 3
	s_cbranch_scc0 .Lpairs_loop
	v_lshl_or_b32 v70, v68, 7, v76
	v_lshl_or_b32 v71, v69, 7, v76
	global_load_dwordx4 v[36:39], v70, s[4:5]
	global_load_dwordx4 v[40:43], v70, s[4:5] offset:64
	global_load_dwordx4 v[44:47], v71, s[4:5]
	global_load_dwordx4 v[48:51], v71, s[4:5] offset:64
	s_branch .Lpairs_loop

	.amdhsa_kernel _ZN12_GLOBAL__N_17k_pairsEPKDF16_PKiS1_PKfS5_S5_Pf
		.amdhsa_group_segment_fixed_size 16384
		.amdhsa_private_segment_fixed_size 0
		.amdhsa_kernarg_size 56
		.amdhsa_user_sgpr_count 2
		.amdhsa_user_sgpr_dispatch_ptr 0
		.amdhsa_user_sgpr_queue_ptr 0
		.amdhsa_user_sgpr_kernarg_segment_ptr 1
		.amdhsa_user_sgpr_dispatch_id 0
		.amdhsa_user_sgpr_kernarg_preload_length 0
		.amdhsa_user_sgpr_kernarg_preload_offset 0
		.amdhsa_user_sgpr_private_segment_size 0
		.amdhsa_uses_dynamic_stack 0
		.amdhsa_enable_private_segment 0
		.amdhsa_system_sgpr_workgroup_id_x 1
		.amdhsa_system_sgpr_workgroup_id_y 0
		.amdhsa_system_sgpr_workgroup_id_z 0
		.amdhsa_system_sgpr_workgroup_info 0
		.amdhsa_system_vgpr_workitem_id 0
		.amdhsa_next_free_vgpr 78
		.amdhsa_next_free_sgpr 40
		.amdhsa_accum_offset 80
		.amdhsa_reserve_vcc 1
		.amdhsa_float_round_mode_32 0
		.amdhsa_float_round_mode_16_64 0
		.amdhsa_float_denorm_mode_32 3
		.amdhsa_float_denorm_mode_16_64 3
		.amdhsa_dx10_clamp 1
		.amdhsa_ieee_mode 1
		.amdhsa_fp16_overflow 0
		.amdhsa_tg_split 0
		.amdhsa_exception_fp_ieee_invalid_op 0
		.amdhsa_exception_fp_denorm_src 0
		.amdhsa_exception_fp_ieee_div_zero 0
		.amdhsa_exception_fp_ieee_overflow 0
		.amdhsa_exception_fp_ieee_underflow 0
		.amdhsa_exception_fp_ieee_inexact 0
		.amdhsa_exception_int_div_zero 0
	.end_amdhsa_kernel

amdhsa.kernels:
  - .agpr_count:     0
    .args:
      - .actual_access:  read_only
        .address_space:  global
        .offset:         0
        .size:           8
        .value_kind:     global_buffer
      - .actual_access:  read_only
        .address_space:  global
        .offset:         8
        .size:           8
        .value_kind:     global_buffer
      - .actual_access:  read_only
        .address_space:  global
        .offset:         16
        .size:           8
        .value_kind:     global_buffer
      - .actual_access:  read_only
        .address_space:  global
        .offset:         24
        .size:           8
        .value_kind:     global_buffer
      - .actual_access:  read_only
        .address_space:  global
        .offset:         32
        .size:           8
        .value_kind:     global_buffer
      - .actual_access:  read_only
        .address_space:  global
        .offset:         40
        .size:           8
        .value_kind:     global_buffer
      - .actual_access:  read_only
        .address_space:  global
        .offset:         48
        .size:           8
        .value_kind:     global_buffer
      - .actual_access:  read_only
        .address_space:  global
        .offset:         56
        .size:           8
        .value_kind:     global_buffer
      - .actual_access:  read_only
        .address_space:  global
        .offset:         64
        .size:           8
        .value_kind:     global_buffer
      - .actual_access:  read_only
        .address_space:  global
        .offset:         72
        .size:           8
        .value_kind:     global_buffer
      - .actual_access:  read_only
        .address_space:  global
        .offset:         80
        .size:           8
        .value_kind:     global_buffer
      - .actual_access:  read_only
        .address_space:  global
        .offset:         88
        .size:           8
        .value_kind:     global_buffer
      - .actual_access:  write_only
        .address_space:  global
        .offset:         96
        .size:           8
        .value_kind:     global_buffer
      - .actual_access:  write_only
        .address_space:  global
        .offset:         104
        .size:           8
        .value_kind:     global_buffer
      - .actual_access:  write_only
        .address_space:  global
        .offset:         112
        .size:           8
        .value_kind:     global_buffer
      - .actual_access:  write_only
        .address_space:  global
        .offset:         120
        .size:           8
        .value_kind:     global_buffer
      - .actual_access:  write_only
        .address_space:  global
        .offset:         128
        .size:           8
        .value_kind:     global_buffer
      - .actual_access:  write_only
        .address_space:  global
        .offset:         136
        .size:           8
        .value_kind:     global_buffer
      - .actual_access:  read_only
        .address_space:  global
        .offset:         144
        .size:           8
        .value_kind:     global_buffer
      - .actual_access:  read_only
        .address_space:  global
        .offset:         152
        .size:           8
        .value_kind:     global_buffer
      - .actual_access:  read_only
        .address_space:  global
        .offset:         160
        .size:           8
        .value_kind:     global_buffer
      - .actual_access:  write_only
        .address_space:  global
        .offset:         168
        .size:           8
        .value_kind:     global_buffer
    .group_segment_fixed_size: 4272
    .kernarg_segment_align: 8
    .kernarg_segment_size: 176
    .language:       OpenCL C
    .language_version:
      - 2
      - 0
    .max_flat_workgroup_size: 256
    .name:           _ZN12_GLOBAL__N_16k_prepEPKfPKiS1_S1_S1_S1_S1_S1_S1_S1_S1_S1_P15HIP_vector_typeIjLj4EEPiPfPDF16_S9_S9_S1_S1_S1_S8_
    .private_segment_fixed_size: 0
    .sgpr_count:     30
    .sgpr_spill_count: 0
    .symbol:         _ZN12_GLOBAL__N_16k_prepEPKfPKiS1_S1_S1_S1_S1_S1_S1_S1_S1_S1_P15HIP_vector_typeIjLj4EEPiPfPDF16_S9_S9_S1_S1_S1_S8_.kd
    .uniform_work_group_size: 1
    .uses_dynamic_stack: false
    .vgpr_count:     144
    .vgpr_spill_count: 0
    .wavefront_size: 64
  - .agpr_count:     0
    .args:
      - .actual_access:  read_only
        .address_space:  global
        .offset:         0
        .size:           8
        .value_kind:     global_buffer
      - .actual_access:  read_only
        .address_space:  global
        .offset:         8
        .size:           8
        .value_kind:     global_buffer
      - .actual_access:  write_only
        .address_space:  global
        .offset:         16
        .size:           8
        .value_kind:     global_buffer
      - .actual_access:  write_only
        .address_space:  global
        .offset:         24
        .size:           8
        .value_kind:     global_buffer
      - .actual_access:  read_only
        .address_space:  global
        .offset:         32
        .size:           8
        .value_kind:     global_buffer
      - .actual_access:  read_only
        .address_space:  global
        .offset:         40
        .size:           8
        .value_kind:     global_buffer
      - .actual_access:  write_only
        .address_space:  global
        .offset:         48
        .size:           8
        .value_kind:     global_buffer
      - .actual_access:  write_only
        .address_space:  global
        .offset:         56
        .size:           8
        .value_kind:     global_buffer
      - .actual_access:  write_only
        .address_space:  global
        .offset:         64
        .size:           8
        .value_kind:     global_buffer
    .group_segment_fixed_size: 7268
    .kernarg_segment_align: 8
    .kernarg_segment_size: 72
    .language:       OpenCL C
    .language_version:
      - 2
      - 0
    .max_flat_workgroup_size: 1024
    .name:           _ZN12_GLOBAL__N_18k_bucketEPK15HIP_vector_typeIjLj4EEPKiPiPS1_PKfS9_PDF16_PfSB_
    .private_segment_fixed_size: 0
    .sgpr_count:     32
    .sgpr_spill_count: 0
    .symbol:         _ZN12_GLOBAL__N_18k_bucketEPK15HIP_vector_typeIjLj4EEPKiPiPS1_PKfS9_PDF16_PfSB_.kd
    .uniform_work_group_size: 1
    .uses_dynamic_stack: false
    .vgpr_count:     62
    .vgpr_spill_count: 0
    .wavefront_size: 64
  - .agpr_count:     0
    .args:
      - .actual_access:  read_only
        .address_space:  global
        .offset:         0
        .size:           8
        .value_kind:     global_buffer
      - .actual_access:  read_only
        .address_space:  global
        .offset:         8
        .size:           8
        .value_kind:     global_buffer
      - .actual_access:  read_only
        .address_space:  global
        .offset:         16
        .size:           8
        .value_kind:     global_buffer
      - .actual_access:  read_only
        .address_space:  global
        .offset:         24
        .size:           8
        .value_kind:     global_buffer
      - .actual_access:  read_only
        .address_space:  global
        .offset:         32
        .size:           8
        .value_kind:     global_buffer
      - .actual_access:  read_only
        .address_space:  global
        .offset:         40
        .size:           8
        .value_kind:     global_buffer
      - .actual_access:  read_only
        .address_space:  global
        .offset:         48
        .size:           8
        .value_kind:     global_buffer
      - .actual_access:  read_only
        .address_space:  global
        .offset:         56
        .size:           8
        .value_kind:     global_buffer
      - .actual_access:  read_only
        .address_space:  global
        .offset:         64
        .size:           8
        .value_kind:     global_buffer
      - .actual_access:  read_only
        .address_space:  global
        .offset:         72
        .size:           8
        .value_kind:     global_buffer
      - .actual_access:  write_only
        .address_space:  global
        .offset:         80
        .size:           8
        .value_kind:     global_buffer
      - .actual_access:  write_only
        .address_space:  global
        .offset:         88
        .size:           8
        .value_kind:     global_buffer
      - .actual_access:  write_only
        .address_space:  global
        .offset:         96
        .size:           8
        .value_kind:     global_buffer
      - .actual_access:  read_only
        .address_space:  global
        .offset:         104
        .size:           8
        .value_kind:     global_buffer
    .group_segment_fixed_size: 25216
    .kernarg_segment_align: 8
    .kernarg_segment_size: 112
    .language:       OpenCL C
    .language_version:
      - 2
      - 0
    .max_flat_workgroup_size: 256
    .name:           _ZN12_GLOBAL__N_18k_layer1EPKDF16_PKfS3_PKiPK15HIP_vector_typeIjLj4EES1_S3_S1_S3_S3_PDF16_PfSB_S3_
    .private_segment_fixed_size: 0
    .sgpr_count:     106
    .sgpr_spill_count: 0
    .symbol:         _ZN12_GLOBAL__N_18k_layer1EPKDF16_PKfS3_PKiPK15HIP_vector_typeIjLj4EES1_S3_S1_S3_S3_PDF16_PfSB_S3_.kd
    .uniform_work_group_size: 1
    .uses_dynamic_stack: false
    .vgpr_count:     96
    .vgpr_spill_count: 0
    .wavefront_size: 64
  - .agpr_count:     0
    .args:
      - .actual_access:  read_only
        .address_space:  global
        .offset:         0
        .size:           8
        .value_kind:     global_buffer
      - .actual_access:  read_only
        .address_space:  global
        .offset:         8
        .size:           8
        .value_kind:     global_buffer
      - .actual_access:  read_only
        .address_space:  global
        .offset:         16
        .size:           8
        .value_kind:     global_buffer
      - .actual_access:  read_only
        .address_space:  global
        .offset:         24
        .size:           8
        .value_kind:     global_buffer
      - .actual_access:  read_only
        .address_space:  global
        .offset:         32
        .size:           8
        .value_kind:     global_buffer
      - .actual_access:  read_only
        .address_space:  global
        .offset:         40
        .size:           8
        .value_kind:     global_buffer
      - .actual_access:  read_only
        .address_space:  global
        .offset:         48
        .size:           8
        .value_kind:     global_buffer
      - .actual_access:  write_only
        .address_space:  global
        .offset:         56
        .size:           8
        .value_kind:     global_buffer
    .group_segment_fixed_size: 6144
    .kernarg_segment_align: 8
    .kernarg_segment_size: 64
    .language:       OpenCL C
    .language_version:
      - 2
      - 0
    .max_flat_workgroup_size: 256
    .name:           _ZN12_GLOBAL__N_18k_layer2EPKDF16_PKfS3_PKiPK15HIP_vector_typeIjLj4EES3_S3_PDF16_
    .private_segment_fixed_size: 0
    .sgpr_count:     42
    .sgpr_spill_count: 0
    .symbol:         _ZN12_GLOBAL__N_18k_layer2EPKDF16_PKfS3_PKiPK15HIP_vector_typeIjLj4EES3_S3_PDF16_.kd
    .uniform_work_group_size: 1
    .uses_dynamic_stack: false
    .vgpr_count:     70
    .vgpr_spill_count: 0
    .wavefront_size: 64
  - .agpr_count:     0
    .args:
      - .actual_access:  read_only
        .address_space:  global
        .offset:         0
        .size:           8
        .value_kind:     global_buffer
      - .actual_access:  read_only
        .address_space:  global
        .offset:         8
        .size:           8
        .value_kind:     global_buffer
      - .actual_access:  read_only
        .address_space:  global
        .offset:         16
        .size:           8
        .value_kind:     global_buffer
      - .actual_access:  read_only
        .address_space:  global
        .offset:         24
        .size:           8
        .value_kind:     global_buffer
      - .actual_access:  read_only
        .address_space:  global
        .offset:         32
        .size:           8
        .value_kind:     global_buffer
      - .actual_access:  read_only
        .address_space:  global
        .offset:         40
        .size:           8
        .value_kind:     global_buffer
      - .actual_access:  write_only
        .address_space:  global
        .offset:         48
        .size:           8
        .value_kind:     global_buffer
    .group_segment_fixed_size: 16384
    .kernarg_segment_align: 8
    .kernarg_segment_size: 56
    .language:       OpenCL C
    .language_version:
      - 2
      - 0
    .max_flat_workgroup_size: 512
    .name:           _ZN12_GLOBAL__N_17k_pairsEPKDF16_PKiS1_PKfS5_S5_Pf
    .private_segment_fixed_size: 0
    .sgpr_count:     46
    .sgpr_spill_count: 0
    .symbol:         _ZN12_GLOBAL__N_17k_pairsEPKDF16_PKiS1_PKfS5_S5_Pf.kd
    .uniform_work_group_size: 1
    .uses_dynamic_stack: false
    .vgpr_count:     78
    .vgpr_spill_count: 0
    .wavefront_size: 64
